# adds the batched rel-pos bias staging (one memory round trip at attention-phase start) with skipped padding so all later code keeps its 256-byte alignment
# baseline (speedup 1.0000x reference)
; #define GAS __attribute__((address_space(1)))
; #define LAS __attribute__((address_space(3)))
; __device__ __forceinline__ int lane_id() { return (int)__builtin_amdgcn_mbcnt_hi(~0u, __builtin_amdgcn_mbcnt_lo(~0u, 0u)); }
; __global__ void __launch_bounds__(NWAVES * 64, 2) hybrid_fwd(Args args) {
;     ...
;             LAS float* biasL = (LAS float*)(F.lds + RING_OFF + A_BIAS);
;             int tid2 = F.wave * 64 + lane_id(); asm volatile("" : "+v"(tid2));
;             for (int i = tid2; i < NH * 257; i += NWAVES * 64) biasL[i] = *(const GAS float*)(F.rel_bias + (size_t)l * NH * 257 + i) * LOG2E;
.LBB0_462:
	s_andn2_b64 vcc, exec, s[0:1]
	s_cbranch_vccnz .LBB0_628
	v_mov_b32_e32 v0, v212
	s_movk_i32 s0, 0x808
	s_nop 0
	v_cmp_gt_i32_e32 vcc, s0, v0
	s_and_saveexec_b64 s[0:1], vcc
	s_cbranch_execz .LBB0_476
	s_waitcnt lgkmcnt(0)
	v_readlane_b32 s4, v250, 36
	v_readlane_b32 s18, v252, 12
	v_readlane_b32 s19, v252, 13
	v_lshlrev_b32_e32 v1, 2, v0
	s_nop 3
	s_mul_i32 s96, s4, 0x808
	s_lshl_b64 s[4:5], s[96:97], 2
	s_add_u32 s8, s18, s4
	s_addc_u32 s9, s19, s5
	v_readlane_b32 s4, v250, 4
	v_add_u32_e32 v6, 0x1000, v1
	v_add_u32_e32 v7, 0x2000, v1
	global_load_dword v2, v1, s[8:9]
	global_load_dword v3, v1, s[8:9] offset:2048
	global_load_dword v4, v6, s[8:9]
	global_load_dword v5, v6, s[8:9] offset:2048
	v_cmp_gt_u32_e32 vcc, 8, v0
	s_and_saveexec_b64 s[2:3], vcc
	global_load_dword v8, v7, s[8:9]
	s_or_b64 exec, exec, s[2:3]
	v_add_u32_e32 v9, s4, v1
	s_mov_b32 s6, 0x3fb8aa3b
	s_waitcnt vmcnt(0)
	v_mul_f32_e32 v2, s6, v2
	v_mul_f32_e32 v3, s6, v3
	v_mul_f32_e32 v4, s6, v4
	v_mul_f32_e32 v5, s6, v5
	ds_write_b32 v9, v2
	ds_write_b32 v9, v3 offset:2048
	ds_write_b32 v9, v4 offset:4096
	ds_write_b32 v9, v5 offset:6144
	s_and_saveexec_b64 s[2:3], vcc
	v_mul_f32_e32 v8, s6, v8
	ds_write_b32 v9, v8 offset:8192
	s_or_b64 exec, exec, s[2:3]
	s_branch .LBB0_476
	s_nop 0
	s_nop 0
	s_nop 0
	s_nop 0
	s_nop 0
	s_nop 0
	s_nop 0
	s_nop 0
	s_nop 0
	s_nop 0
	s_nop 0
	s_nop 0
	s_nop 0
	s_nop 0
	s_nop 0
	s_nop 0
	s_nop 0
	s_nop 0
	s_nop 0
	s_nop 0
	s_nop 0
	s_nop 0
	s_nop 0
	s_nop 0
	s_nop 0
	s_nop 0
	s_nop 0
